# router: next tile h rows staged right after the logits k-loop (overlaps reduction, U write, top-k), fragments 3 k-steps ahead
# speedup vs baseline: 1.0381x; 1.0022x over previous
; #define RT_LOADH(tile_) do { const float* hp_ = H + (size_t)((tile_) * 16 + n) * D + wave * 256 + 8 * q; _Pragma("unroll") for (int ks = 0; ks < 8; ++ks) { hv[ks][0] = *(const f32x4*)(hp_ + ks * 32); hv[ks][1] = *(const f32x4*)(hp_ + ks * 32 + 4); } } while (0)
; DI void phase_router(const Args& a, int l, LAS unsigned char* lds, int wave, int lane, int bid, int G, bool dummy = false) {
;     ...
;     if (bid < T / 16) RT_LOADH(bid);
.Lrouter_all_tiles:
	s_cmpk_lt_i32 s1, 0x204
	s_waitcnt vmcnt(9)
	v_and_b32_e32 v97, 15, v68
	s_cselect_b64 s[8:9], -1, 0
	s_cmpk_gt_i32 s1, 0x203
	v_lshlrev_b32_e32 v67, 3, v66
	s_cbranch_scc1 .LBB0_1638
	s_waitcnt vmcnt(7)
	v_lshl_or_b32 v2, s1, 4, v97
	v_ashrrev_i32_e32 v3, 31, v2
	v_lshlrev_b64 v[2:3], 13, v[2:3]
	v_lshl_add_u64 v[2:3], s[4:5], 0, v[2:3]
	v_lshl_add_u64 v[2:3], s[28:29], 2, v[2:3]
	v_lshlrev_b32_e32 v90, 2, v67
	s_waitcnt vmcnt(0)
	v_lshl_add_u64 v[54:55], v[2:3], 0, v[90:91]
	global_load_dwordx4 v[110:113], v[54:55], off offset:16
	global_load_dwordx4 v[114:117], v[54:55], off
	global_load_dwordx4 v[118:121], v[54:55], off offset:144
	global_load_dwordx4 v[122:125], v[54:55], off offset:128
	global_load_dwordx4 v[126:129], v[54:55], off offset:272
	global_load_dwordx4 v[130:133], v[54:55], off offset:256
	global_load_dwordx4 v[134:137], v[54:55], off offset:400
	global_load_dwordx4 v[138:141], v[54:55], off offset:384
	global_load_dwordx4 v[142:145], v[54:55], off offset:528
	global_load_dwordx4 v[146:149], v[54:55], off offset:512
	global_load_dwordx4 v[150:153], v[54:55], off offset:656
	global_load_dwordx4 v[154:157], v[54:55], off offset:640
	global_load_dwordx4 v[186:189], v[54:55], off offset:784
	global_load_dwordx4 v[182:185], v[54:55], off offset:768
	global_load_dwordx4 v[158:161], v[54:55], off offset:912
	global_load_dwordx4 v[178:181], v[54:55], off offset:896

; #define LAS __attribute__((address_space(3)))
; #define RT_LOADH(tile_) do { const float* hp_ = H + (size_t)((tile_) * 16 + n) * D + wave * 256 + 8 * q; _Pragma("unroll") for (int ks = 0; ks < 8; ++ks) { hv[ks][0] = *(const f32x4*)(hp_ + ks * 32); hv[ks][1] = *(const f32x4*)(hp_ + ks * 32 + 4); } } while (0)
; #define RT_WLOAD(s_, ks_) do { const int k0_ = wave * 256 + (ks_) * 32 + 8 * q; _Pragma("unroll") for (int nt = 0; nt < 5; ++nt) wfr[s_][nt] = *(const bf16x8*)(WRO + (size_t)(nt * 16 + n) * D + k0_); \
;             gfr[s_][0] = *(const f32x4*)(gp + (ks_) * 32); gfr[s_][1] = *(const f32x4*)(gp + (ks_) * 32 + 4); } while (0)
; DI void phase_router(const Args& a, int l, LAS unsigned char* lds, int wave, int lane, int bid, int G, bool dummy = false) {
;     unsigned char* ws = (unsigned char*)a.ws; const float* H = (const float*)(ws + WS_H); bf16* U = (bf16*)(ws + WS_U); const bf16* WRO = (const bf16*)(ws + WS_WRO) + (size_t)l * 80 * D;
;     const float* gain = a.inp(I_NORM_FFN) + (size_t)l * D; const float* bco = a.inp(I_BCOARSE) + l * 8; const float* bfi = a.inp(I_BFINE) + l * 64;
;     int* toke = (int*)(ws + WS_TOKE); int* toks = (int*)(ws + WS_TOKS); float* tokw = (float*)(ws + WS_TOKW); unsigned* cnt = (unsigned*)(ws + WS_CTL) + CW_CNT + l * 64 * 16;
;     int* elist = (int*)(ws + WS_ELIST);
;     if (dummy) { toke = (int*)(ws + WS_XR); toks = toke + 2 * T; tokw = (float*)(toks + 2 * T); cnt += 8192; U = (bf16*)(ws + WS_XR) + (size_t)8 * T; elist = (int*)(ws + WS_XR) + (size_t)(8 + 2048) * T; }
;     LAS float* red = (LAS float*)lds;
;     LAS float* ssp = red + 8 * 16 * 80;
;     LAS float* lg = ssp + 8 * 16;
;     LAS float* rs = lg + 16 * 72;
;     LAS float* bia = rs + 16;
;     const int tid = wave * 64 + lane;
;     const int n = lane & 15, q = lane >> 4;
;     f32x4 hv[8][2];
;     const float* gp = gain + wave * 256 + 8 * q;
;     ...
;     if (bid < T / 16) RT_LOADH(bid);
;     if (wave * 64 + lane < 72) { const int nn_ = wave * 64 + lane; bia[nn_] = (nn_ < 8) ? bco[nn_] : bfi[nn_ - 8]; }
;     for (int tile = bid; tile < T / 16; tile += G) { const int row0 = tile * 16;
;         __syncthreads();
;         f32x4 acc[5];
; #pragma unroll
;         for (int nt = 0; nt < 5; ++nt) acc[nt] = (f32x4){0.f, 0.f, 0.f, 0.f};
;         float ss = 0.f;
;         bf16x8 wfr[2][5]; f32x4 gfr[2][2];
;     ...
;         RT_WLOAD(0, 0);
.LBB0_1640:
	s_or_b64 exec, exec, s[24:25]
	s_andn2_b64 vcc, exec, s[8:9]
	s_cbranch_vccnz .LBB0_1658
	s_lshl_b64 s[8:9], s[28:29], 1
	s_add_u32 s8, s26, s8
	s_addc_u32 s9, s27, s9
	s_lshl_b64 s[34:35], s[28:29], 2
	v_lshlrev_b32_e32 v90, 1, v67
	s_add_u32 s4, s4, s34
	v_lshl_add_u64 v[70:71], s[8:9], 0, v[90:91]
	s_addc_u32 s5, s5, s35
	v_lshlrev_b32_e32 v90, 2, v67
	v_readlane_b32 s38, v255, 30
	s_waitcnt vmcnt(4)
	v_lshl_add_u64 v[92:93], s[4:5], 0, v[90:91]
	s_mul_i32 s4, s38, 0x50000
	s_add_u32 s36, s26, s4
	s_addc_u32 s37, s27, 0
	s_add_u32 s4, s26, 0x39e31000
	s_mov_b64 s[8:9], 0x4300000
	s_addc_u32 s5, s27, 0
	v_lshl_add_u64 v[88:89], v[70:71], 0, s[8:9]
	s_add_u32 s8, s26, 0x39e41200
	s_addc_u32 s9, s27, 0
	s_add_u32 s12, s26, 0x39e51400
	s_addc_u32 s13, s27, 0
	s_lshl_b32 s94, s38, 10
	s_lshl_b64 s[24:25], s[94:95], 2
	s_add_u32 s24, s26, s24
	s_addc_u32 s25, s27, s25
	s_add_u32 s24, s24, 0x10000
	v_readlane_b32 s39, v255, 31
	s_addc_u32 s25, s25, 0
	s_mov_b32 s39, s95
	s_add_u32 s26, s26, 0x39e61600
	s_addc_u32 s27, s27, 0
	s_mov_b32 s40, s38
	s_lshl_b64 s[38:39], s[38:39], 13
	s_waitcnt lgkmcnt(0)
	s_add_u32 s2, s2, s38
	s_addc_u32 s3, s3, s39
	s_add_u32 s2, s2, s34
	v_or_b32_e32 v70, s28, v67
	v_and_b32_e32 v69, 64, v218
	s_addc_u32 s3, s3, s35
	v_ashrrev_i32_e32 v71, 31, v70
	v_xor_b32_e32 v67, 16, v218
	v_add_u32_e32 v69, 64, v69
	v_lshl_add_u64 v[94:95], s[2:3], 0, v[90:91]
	v_lshl_add_u64 v[70:71], v[70:71], 1, s[36:37]
	s_mov_b64 s[2:3], 0x40697200
	v_cmp_lt_i32_e32 vcc, v67, v69
	v_lshl_add_u64 v[72:73], v[70:71], 0, s[2:3]
	s_add_i32 s2, s30, 0
	v_cndmask_b32_e32 v67, v218, v67, vcc
	v_lshlrev_b32_e32 v87, 2, v67
	v_xor_b32_e32 v67, 32, v218
	v_lshl_add_u32 v175, v68, 2, s2
	s_movk_i32 s2, 0x480
	v_cmp_lt_i32_e32 vcc, v67, v69
	v_lshl_add_u32 v96, v86, 2, 0
	v_cmp_gt_i32_e64 s[42:43], s2, v86
	s_movk_i32 s2, 0x11c
	v_cndmask_b32_e32 v67, v218, v67, vcc
	v_lshlrev_b32_e32 v66, 2, v66
	v_mad_u64_u32 v[98:99], s[2:3], v86, s2, v[96:97]
	v_lshlrev_b32_e32 v90, 12, v97
	v_lshlrev_b32_e32 v174, 2, v67
	v_cmp_gt_u32_e64 s[38:39], 16, v68
	v_lshl_or_b32 v76, s7, 4, v66
	s_waitcnt vmcnt(1)
	v_lshl_add_u64 v[100:101], v[72:73], 0, v[90:91]
	v_or_b32_e32 v66, 0x10000, v90
	v_mov_b32_e32 v67, v91
	v_or_b32_e32 v68, 0x20000, v90
	v_mov_b32_e32 v69, v91
	v_or_b32_e32 v74, 0x30000, v90
	v_mov_b32_e32 v75, v91
	v_or_b32_e32 v90, 0x40000, v90
	s_mov_b64 s[2:3], 0x40697240
	v_lshl_add_u64 v[102:103], v[72:73], 0, v[66:67]
	v_lshl_add_u64 v[104:105], v[72:73], 0, v[68:69]
	v_lshl_add_u64 v[106:107], v[72:73], 0, v[74:75]
	s_waitcnt vmcnt(0)
	v_lshl_add_u64 v[108:109], v[72:73], 0, v[90:91]
	v_lshl_add_u64 v[72:73], v[70:71], 0, s[2:3]
	s_mov_b64 s[2:3], 0x40697280
	v_lshl_add_u64 v[72:73], v[70:71], 0, s[2:3]
	s_mov_b64 s[2:3], 0x406972c0
	v_lshl_add_u64 v[72:73], v[70:71], 0, s[2:3]
	s_mov_b64 s[2:3], 0x40697300
	v_lshl_add_u64 v[72:73], v[70:71], 0, s[2:3]
	s_mov_b64 s[2:3], 0x40697340
	v_lshl_add_u64 v[72:73], v[70:71], 0, s[2:3]
	s_mov_b64 s[2:3], 0x40697380
	v_lshl_add_u64 v[72:73], v[70:71], 0, s[2:3]
	s_mov_b64 s[2:3], 0x406973c0
	v_lshl_add_u64 v[70:71], v[70:71], 0, s[2:3]
	s_movk_i32 s2, 0x140
	v_writelane_b32 v255, s40, 30
	v_lshl_add_u32 v176, v97, 2, 0
	v_mul_lo_u32 v66, v76, s2
	v_writelane_b32 v255, s41, 31
	v_cmp_gt_i32_e64 s[40:41], 16, v86
	v_add_u32_e32 v99, v176, v66
	s_branch .LBB0_1645

; DI unsigned pk2(float a, float b) { f32x2 v = {a, b}; bf16x2_t r = __builtin_convertvector(v, bf16x2_t); return __builtin_bit_cast(unsigned, r); }
; #define RT_WLOAD(s_, ks_) do { const int k0_ = wave * 256 + (ks_) * 32 + 8 * q; _Pragma("unroll") for (int nt = 0; nt < 5; ++nt) wfr[s_][nt] = *(const bf16x8*)(WRO + (size_t)(nt * 16 + n) * D + k0_); \
;             gfr[s_][0] = *(const f32x4*)(gp + (ks_) * 32); gfr[s_][1] = *(const f32x4*)(gp + (ks_) * 32 + 4); } while (0)
; DI void phase_router(const Args& a, int l, LAS unsigned char* lds, int wave, int lane, int bid, int G, bool dummy = false) {
;     ...
;     for (int tile = bid; tile < T / 16; tile += G) { const int row0 = tile * 16;
;         __syncthreads();
;         f32x4 acc[5];
; #pragma unroll
;         for (int nt = 0; nt < 5; ++nt) acc[nt] = (f32x4){0.f, 0.f, 0.f, 0.f};
;         float ss = 0.f;
;         bf16x8 wfr[2][5]; f32x4 gfr[2][2];
;     ...
;         RT_WLOAD(0, 0);
; #pragma unroll
;         for (int ks = 0; ks < 8; ++ks) {
;             if (ks < 7) RT_WLOAD((ks + 1) & 1, ks + 1);
;             __builtin_amdgcn_sched_barrier(0);
;             const f32x4 g0 = gfr[ks & 1][0], g1 = gfr[ks & 1][1]; const f32x4 x0 = hv[ks][0], x1 = hv[ks][1];
;             ss += (x0[0] * x0[0] + x0[1] * x0[1]) + (x0[2] * x0[2] + x0[3] * x0[3]) + (x1[0] * x1[0] + x1[1] * x1[1]) + (x1[2] * x1[2] + x1[3] * x1[3]);
;             const f32x4 y0 = x0 * g0, y1 = x1 * g1; hv[ks][0] = y0; hv[ks][1] = y1; u32x4 aw;     aw.x = pk2(y0[0], y0[1]); aw.y = pk2(y0[2], y0[3]); aw.z = pk2(y1[0], y1[1]); aw.w = pk2(y1[2], y1[3]);
;             const bf16x8 af = __builtin_bit_cast(bf16x8, aw);
; #pragma unroll
;             for (int nt = 0; nt < 5; ++nt) acc[nt] = __builtin_amdgcn_mfma_f32_16x16x32_bf16(af, wfr[ks & 1][nt], acc[nt], 0, 0, 0);
;             __builtin_amdgcn_sched_barrier(0); }
.LBB0_1645:
	s_waitcnt vmcnt(0)
	v_mov_b64_e32 v[2:3], v[110:111]
	v_mov_b64_e32 v[4:5], v[112:113]
	v_mov_b64_e32 v[6:7], v[114:115]
	v_mov_b64_e32 v[8:9], v[116:117]
	v_mov_b64_e32 v[10:11], v[118:119]
	v_mov_b64_e32 v[12:13], v[120:121]
	v_mov_b64_e32 v[14:15], v[122:123]
	v_mov_b64_e32 v[16:17], v[124:125]
	v_mov_b64_e32 v[18:19], v[126:127]
	v_mov_b64_e32 v[20:21], v[128:129]
	v_mov_b64_e32 v[22:23], v[130:131]
	v_mov_b64_e32 v[24:25], v[132:133]
	v_mov_b64_e32 v[26:27], v[134:135]
	v_mov_b64_e32 v[28:29], v[136:137]
	v_mov_b64_e32 v[30:31], v[138:139]
	v_mov_b64_e32 v[32:33], v[140:141]
	v_mov_b64_e32 v[34:35], v[142:143]
	v_mov_b64_e32 v[36:37], v[144:145]
	v_mov_b64_e32 v[38:39], v[146:147]
	v_mov_b64_e32 v[40:41], v[148:149]
	v_mov_b64_e32 v[42:43], v[150:151]
	v_mov_b64_e32 v[44:45], v[152:153]
	v_mov_b64_e32 v[46:47], v[154:155]
	v_mov_b64_e32 v[48:49], v[156:157]
	v_mov_b64_e32 v[50:51], v[158:159]
	v_mov_b64_e32 v[52:53], v[160:161]
	v_mov_b64_e32 v[54:55], v[178:179]
	v_mov_b64_e32 v[56:57], v[180:181]
	v_mov_b64_e32 v[58:59], v[182:183]
	v_mov_b64_e32 v[60:61], v[184:185]
	v_mov_b64_e32 v[62:63], v[186:187]
	v_mov_b64_e32 v[64:65], v[188:189]
	s_barrier
	global_load_dwordx4 v[110:113], v[100:101], off
	global_load_dwordx4 v[114:117], v[102:103], off
	global_load_dwordx4 v[118:121], v[104:105], off
	global_load_dwordx4 v[122:125], v[106:107], off
	global_load_dwordx4 v[126:129], v[108:109], off
	global_load_dwordx4 v[130:133], v[94:95], off
	global_load_dwordx4 v[134:137], v[94:95], off offset:16
	global_load_dwordx4 v[138:141], v[100:101], off offset:64
	global_load_dwordx4 v[142:145], v[102:103], off offset:64
	global_load_dwordx4 v[146:149], v[104:105], off offset:64
	global_load_dwordx4 v[150:153], v[106:107], off offset:64
	global_load_dwordx4 v[154:157], v[108:109], off offset:64
	global_load_dwordx4 v[158:161], v[94:95], off offset:128
	global_load_dwordx4 v[178:181], v[94:95], off offset:144
	global_load_dwordx4 v[182:185], v[100:101], off offset:128
	global_load_dwordx4 v[186:189], v[102:103], off offset:128
	global_load_dwordx4 v[190:193], v[104:105], off offset:128
	global_load_dwordx4 v[194:197], v[106:107], off offset:128
	global_load_dwordx4 v[198:201], v[108:109], off offset:128
	global_load_dwordx4 v[202:205], v[94:95], off offset:256
	global_load_dwordx4 v[206:209], v[94:95], off offset:272
	v_mul_f32_e32 v90, v7, v7
	v_mul_f32_e32 v233, v9, v9
	v_fmac_f32_e32 v90, v6, v6
	v_fmac_f32_e32 v233, v8, v8
	v_add_f32_e32 v90, v90, v233
	v_mul_f32_e32 v233, v3, v3
	v_fmac_f32_e32 v233, v2, v2
	v_add_f32_e32 v90, v233, v90
	v_mul_f32_e32 v233, v5, v5
	v_fmac_f32_e32 v233, v4, v4
	s_waitcnt vmcnt(14)
	v_pk_mul_f32 v[8:9], v[8:9], v[132:133]
	v_pk_mul_f32 v[6:7], v[6:7], v[130:131]
	v_pk_mul_f32 v[4:5], v[4:5], v[136:137]
	v_pk_mul_f32 v[2:3], v[2:3], v[134:135]
	v_cvt_pk_bf16_f32 v164, v6, v7
	v_cvt_pk_bf16_f32 v165, v8, v9
	v_cvt_pk_bf16_f32 v166, v2, v3
	v_cvt_pk_bf16_f32 v167, v4, v5
	v_add_f32_e32 v90, v233, v90
	s_nop 0
	v_mfma_f32_16x16x32_bf16 v[66:69], v[164:167], v[110:113], 0
	v_mfma_f32_16x16x32_bf16 v[78:81], v[164:167], v[114:117], 0
	v_mfma_f32_16x16x32_bf16 v[74:77], v[164:167], v[118:121], 0
	v_mfma_f32_16x16x32_bf16 v[70:73], v[164:167], v[122:125], 0
	v_mfma_f32_16x16x32_bf16 v[82:85], v[164:167], v[126:129], 0
	global_load_dwordx4 v[210:213], v[100:101], off offset:192
	global_load_dwordx4 v[214:217], v[102:103], off offset:192
	global_load_dwordx4 v[234:237], v[104:105], off offset:192
	global_load_dwordx4 v[238:241], v[106:107], off offset:192
	global_load_dwordx4 v[242:245], v[108:109], off offset:192
	global_load_dwordx4 v[246:249], v[94:95], off offset:384
	global_load_dwordx4 v[250:253], v[94:95], off offset:400
	v_mul_f32_e32 v177, v15, v15
	v_mul_f32_e32 v233, v17, v17
	v_fmac_f32_e32 v177, v14, v14
	v_fmac_f32_e32 v233, v16, v16
	v_add_f32_e32 v177, v177, v233
	v_mul_f32_e32 v233, v11, v11
	v_fmac_f32_e32 v233, v10, v10
	v_add_f32_e32 v177, v233, v177
	v_mul_f32_e32 v233, v13, v13
	v_fmac_f32_e32 v233, v12, v12
	s_waitcnt vmcnt(14)
	v_pk_mul_f32 v[16:17], v[16:17], v[160:161]
	v_pk_mul_f32 v[14:15], v[14:15], v[158:159]
	v_pk_mul_f32 v[12:13], v[12:13], v[180:181]
	v_pk_mul_f32 v[10:11], v[10:11], v[178:179]
	v_cvt_pk_bf16_f32 v164, v14, v15
	v_cvt_pk_bf16_f32 v165, v16, v17
	v_cvt_pk_bf16_f32 v166, v10, v11
	v_cvt_pk_bf16_f32 v167, v12, v13
	v_add_f32_e32 v177, v233, v177
	v_add_f32_e32 v90, v177, v90
	v_mfma_f32_16x16x32_bf16 v[66:69], v[164:167], v[138:141], v[66:69]
	v_mfma_f32_16x16x32_bf16 v[78:81], v[164:167], v[142:145], v[78:81]
	v_mfma_f32_16x16x32_bf16 v[74:77], v[164:167], v[146:149], v[74:77]
	v_mfma_f32_16x16x32_bf16 v[70:73], v[164:167], v[150:153], v[70:73]
	v_mfma_f32_16x16x32_bf16 v[82:85], v[164:167], v[154:157], v[82:85]
	global_load_dwordx4 v[110:113], v[100:101], off offset:256
	global_load_dwordx4 v[114:117], v[102:103], off offset:256
	global_load_dwordx4 v[118:121], v[104:105], off offset:256
	global_load_dwordx4 v[122:125], v[106:107], off offset:256
	global_load_dwordx4 v[126:129], v[108:109], off offset:256
	global_load_dwordx4 v[130:133], v[94:95], off offset:512
	global_load_dwordx4 v[134:137], v[94:95], off offset:528
	v_mul_f32_e32 v177, v23, v23
	v_mul_f32_e32 v233, v25, v25
	v_fmac_f32_e32 v177, v22, v22
	v_fmac_f32_e32 v233, v24, v24
	v_add_f32_e32 v177, v177, v233
	v_mul_f32_e32 v233, v19, v19
	v_fmac_f32_e32 v233, v18, v18
	v_add_f32_e32 v177, v233, v177
	v_mul_f32_e32 v233, v21, v21
	v_fmac_f32_e32 v233, v20, v20
	s_waitcnt vmcnt(14)
; DI unsigned pk2(float a, float b) { f32x2 v = {a, b}; bf16x2_t r = __builtin_convertvector(v, bf16x2_t); return __builtin_bit_cast(unsigned, r); }
; #define RT_WLOAD(s_, ks_) do { const int k0_ = wave * 256 + (ks_) * 32 + 8 * q; _Pragma("unroll") for (int nt = 0; nt < 5; ++nt) wfr[s_][nt] = *(const bf16x8*)(WRO + (size_t)(nt * 16 + n) * D + k0_); \
;             gfr[s_][0] = *(const f32x4*)(gp + (ks_) * 32); gfr[s_][1] = *(const f32x4*)(gp + (ks_) * 32 + 4); } while (0)
; DI void phase_router(const Args& a, int l, LAS unsigned char* lds, int wave, int lane, int bid, int G, bool dummy = false) {
;     ...
;         RT_WLOAD(0, 0);
; #pragma unroll
;         for (int ks = 0; ks < 8; ++ks) {
;             if (ks < 7) RT_WLOAD((ks + 1) & 1, ks + 1);
;             __builtin_amdgcn_sched_barrier(0);
;             const f32x4 g0 = gfr[ks & 1][0], g1 = gfr[ks & 1][1]; const f32x4 x0 = hv[ks][0], x1 = hv[ks][1];
;             ss += (x0[0] * x0[0] + x0[1] * x0[1]) + (x0[2] * x0[2] + x0[3] * x0[3]) + (x1[0] * x1[0] + x1[1] * x1[1]) + (x1[2] * x1[2] + x1[3] * x1[3]);
;             const f32x4 y0 = x0 * g0, y1 = x1 * g1; hv[ks][0] = y0; hv[ks][1] = y1; u32x4 aw;     aw.x = pk2(y0[0], y0[1]); aw.y = pk2(y0[2], y0[3]); aw.z = pk2(y1[0], y1[1]); aw.w = pk2(y1[2], y1[3]);
;             const bf16x8 af = __builtin_bit_cast(bf16x8, aw);
; #pragma unroll
;             for (int nt = 0; nt < 5; ++nt) acc[nt] = __builtin_amdgcn_mfma_f32_16x16x32_bf16(af, wfr[ks & 1][nt], acc[nt], 0, 0, 0);
;             __builtin_amdgcn_sched_barrier(0); }
	v_pk_mul_f32 v[24:25], v[24:25], v[204:205]
	v_pk_mul_f32 v[22:23], v[22:23], v[202:203]
	v_pk_mul_f32 v[20:21], v[20:21], v[208:209]
	v_pk_mul_f32 v[18:19], v[18:19], v[206:207]
	v_cvt_pk_bf16_f32 v164, v22, v23
	v_cvt_pk_bf16_f32 v165, v24, v25
	v_cvt_pk_bf16_f32 v166, v18, v19
	v_cvt_pk_bf16_f32 v167, v20, v21
	v_add_f32_e32 v177, v233, v177
	v_add_f32_e32 v90, v177, v90
	v_mfma_f32_16x16x32_bf16 v[66:69], v[164:167], v[182:185], v[66:69]
	v_mfma_f32_16x16x32_bf16 v[78:81], v[164:167], v[186:189], v[78:81]
	v_mfma_f32_16x16x32_bf16 v[74:77], v[164:167], v[190:193], v[74:77]
	v_mfma_f32_16x16x32_bf16 v[70:73], v[164:167], v[194:197], v[70:73]
	v_mfma_f32_16x16x32_bf16 v[82:85], v[164:167], v[198:201], v[82:85]
	global_load_dwordx4 v[138:141], v[100:101], off offset:320
	global_load_dwordx4 v[142:145], v[102:103], off offset:320
	global_load_dwordx4 v[146:149], v[104:105], off offset:320
	global_load_dwordx4 v[150:153], v[106:107], off offset:320
	global_load_dwordx4 v[154:157], v[108:109], off offset:320
	global_load_dwordx4 v[158:161], v[94:95], off offset:640
	global_load_dwordx4 v[178:181], v[94:95], off offset:656
	v_mul_f32_e32 v177, v31, v31
	v_mul_f32_e32 v233, v33, v33
	v_fmac_f32_e32 v177, v30, v30
	v_fmac_f32_e32 v233, v32, v32
	v_add_f32_e32 v177, v177, v233
	v_mul_f32_e32 v233, v27, v27
	v_fmac_f32_e32 v233, v26, v26
	v_add_f32_e32 v177, v233, v177
	v_mul_f32_e32 v233, v29, v29
	v_fmac_f32_e32 v233, v28, v28
	s_waitcnt vmcnt(14)
	v_pk_mul_f32 v[32:33], v[32:33], v[248:249]
	v_pk_mul_f32 v[30:31], v[30:31], v[246:247]
	v_pk_mul_f32 v[28:29], v[28:29], v[252:253]
	v_pk_mul_f32 v[26:27], v[26:27], v[250:251]
	v_cvt_pk_bf16_f32 v164, v30, v31
	v_cvt_pk_bf16_f32 v165, v32, v33
	v_cvt_pk_bf16_f32 v166, v26, v27
	v_cvt_pk_bf16_f32 v167, v28, v29
	v_add_f32_e32 v177, v233, v177
	v_add_f32_e32 v90, v177, v90
	v_mfma_f32_16x16x32_bf16 v[66:69], v[164:167], v[210:213], v[66:69]
	v_mfma_f32_16x16x32_bf16 v[78:81], v[164:167], v[214:217], v[78:81]
	v_mfma_f32_16x16x32_bf16 v[74:77], v[164:167], v[234:237], v[74:77]
	v_mfma_f32_16x16x32_bf16 v[70:73], v[164:167], v[238:241], v[70:73]
	v_mfma_f32_16x16x32_bf16 v[82:85], v[164:167], v[242:245], v[82:85]
	global_load_dwordx4 v[182:185], v[100:101], off offset:384
	global_load_dwordx4 v[186:189], v[102:103], off offset:384
	global_load_dwordx4 v[190:193], v[104:105], off offset:384
	global_load_dwordx4 v[194:197], v[106:107], off offset:384
	global_load_dwordx4 v[198:201], v[108:109], off offset:384
	global_load_dwordx4 v[202:205], v[94:95], off offset:768
	global_load_dwordx4 v[206:209], v[94:95], off offset:784
	v_mul_f32_e32 v177, v39, v39
	v_mul_f32_e32 v233, v41, v41
	v_fmac_f32_e32 v177, v38, v38
	v_fmac_f32_e32 v233, v40, v40
	v_add_f32_e32 v177, v177, v233
	v_mul_f32_e32 v233, v35, v35
	v_fmac_f32_e32 v233, v34, v34
	v_add_f32_e32 v177, v233, v177
	v_mul_f32_e32 v233, v37, v37
	v_fmac_f32_e32 v233, v36, v36
	s_waitcnt vmcnt(14)
	v_pk_mul_f32 v[40:41], v[40:41], v[132:133]
	v_pk_mul_f32 v[38:39], v[38:39], v[130:131]
	v_pk_mul_f32 v[36:37], v[36:37], v[136:137]
	v_pk_mul_f32 v[34:35], v[34:35], v[134:135]
	v_cvt_pk_bf16_f32 v164, v38, v39
	v_cvt_pk_bf16_f32 v165, v40, v41
	v_cvt_pk_bf16_f32 v166, v34, v35
	v_cvt_pk_bf16_f32 v167, v36, v37
	v_add_f32_e32 v177, v233, v177
	v_add_f32_e32 v90, v177, v90
	v_mfma_f32_16x16x32_bf16 v[66:69], v[164:167], v[110:113], v[66:69]
	v_mfma_f32_16x16x32_bf16 v[78:81], v[164:167], v[114:117], v[78:81]
	v_mfma_f32_16x16x32_bf16 v[74:77], v[164:167], v[118:121], v[74:77]
	v_mfma_f32_16x16x32_bf16 v[70:73], v[164:167], v[122:125], v[70:73]
	v_mfma_f32_16x16x32_bf16 v[82:85], v[164:167], v[126:129], v[82:85]
	global_load_dwordx4 v[210:213], v[100:101], off offset:448
	global_load_dwordx4 v[214:217], v[102:103], off offset:448
	global_load_dwordx4 v[234:237], v[104:105], off offset:448
	global_load_dwordx4 v[238:241], v[106:107], off offset:448
	global_load_dwordx4 v[242:245], v[108:109], off offset:448
	global_load_dwordx4 v[246:249], v[94:95], off offset:896
	global_load_dwordx4 v[250:253], v[94:95], off offset:912
	v_mul_f32_e32 v177, v47, v47
	v_mul_f32_e32 v233, v49, v49
	v_fmac_f32_e32 v177, v46, v46
	v_fmac_f32_e32 v233, v48, v48
	v_add_f32_e32 v177, v177, v233
	v_mul_f32_e32 v233, v43, v43
	v_fmac_f32_e32 v233, v42, v42
	v_add_f32_e32 v177, v233, v177
	v_mul_f32_e32 v233, v45, v45
	v_fmac_f32_e32 v233, v44, v44
	s_waitcnt vmcnt(14)
; DI unsigned pk2(float a, float b) { f32x2 v = {a, b}; bf16x2_t r = __builtin_convertvector(v, bf16x2_t); return __builtin_bit_cast(unsigned, r); }
; #define RT_LOADH(tile_) do { const float* hp_ = H + (size_t)((tile_) * 16 + n) * D + wave * 256 + 8 * q; _Pragma("unroll") for (int ks = 0; ks < 8; ++ks) { hv[ks][0] = *(const f32x4*)(hp_ + ks * 32); hv[ks][1] = *(const f32x4*)(hp_ + ks * 32 + 4); } } while (0)
; #define RT_WLOAD(s_, ks_) do { const int k0_ = wave * 256 + (ks_) * 32 + 8 * q; _Pragma("unroll") for (int nt = 0; nt < 5; ++nt) wfr[s_][nt] = *(const bf16x8*)(WRO + (size_t)(nt * 16 + n) * D + k0_); \
;             gfr[s_][0] = *(const f32x4*)(gp + (ks_) * 32); gfr[s_][1] = *(const f32x4*)(gp + (ks_) * 32 + 4); } while (0)
; DI void phase_router(const Args& a, int l, LAS unsigned char* lds, int wave, int lane, int bid, int G, bool dummy = false) {
;     ...
; #pragma unroll
;         for (int ks = 0; ks < 8; ++ks) {
;             if (ks < 7) RT_WLOAD((ks + 1) & 1, ks + 1);
;             __builtin_amdgcn_sched_barrier(0);
;             const f32x4 g0 = gfr[ks & 1][0], g1 = gfr[ks & 1][1]; const f32x4 x0 = hv[ks][0], x1 = hv[ks][1];
;             ss += (x0[0] * x0[0] + x0[1] * x0[1]) + (x0[2] * x0[2] + x0[3] * x0[3]) + (x1[0] * x1[0] + x1[1] * x1[1]) + (x1[2] * x1[2] + x1[3] * x1[3]);
;             const f32x4 y0 = x0 * g0, y1 = x1 * g1; hv[ks][0] = y0; hv[ks][1] = y1; u32x4 aw;     aw.x = pk2(y0[0], y0[1]); aw.y = pk2(y0[2], y0[3]); aw.z = pk2(y1[0], y1[1]); aw.w = pk2(y1[2], y1[3]);
;             const bf16x8 af = __builtin_bit_cast(bf16x8, aw);
; #pragma unroll
;             for (int nt = 0; nt < 5; ++nt) acc[nt] = __builtin_amdgcn_mfma_f32_16x16x32_bf16(af, wfr[ks & 1][nt], acc[nt], 0, 0, 0);
;             __builtin_amdgcn_sched_barrier(0); }
;     ...
;         ss += __shfl_xor(ss, 16); ss += __shfl_xor(ss, 32);
;         if (q == 0) ssp[wave * 16 + n] = ss;
;     ...
;         if (tile + G < T / 16) RT_LOADH(tile + G);
	v_pk_mul_f32 v[48:49], v[48:49], v[160:161]
	v_pk_mul_f32 v[46:47], v[46:47], v[158:159]
	v_pk_mul_f32 v[44:45], v[44:45], v[180:181]
	v_pk_mul_f32 v[42:43], v[42:43], v[178:179]
	v_cvt_pk_bf16_f32 v164, v46, v47
	v_cvt_pk_bf16_f32 v165, v48, v49
	v_cvt_pk_bf16_f32 v166, v42, v43
	v_cvt_pk_bf16_f32 v167, v44, v45
	v_add_f32_e32 v177, v233, v177
	v_add_f32_e32 v90, v177, v90
	v_mfma_f32_16x16x32_bf16 v[66:69], v[164:167], v[138:141], v[66:69]
	v_mfma_f32_16x16x32_bf16 v[78:81], v[164:167], v[142:145], v[78:81]
	v_mfma_f32_16x16x32_bf16 v[74:77], v[164:167], v[146:149], v[74:77]
	v_mfma_f32_16x16x32_bf16 v[70:73], v[164:167], v[150:153], v[70:73]
	v_mfma_f32_16x16x32_bf16 v[82:85], v[164:167], v[154:157], v[82:85]
	v_mul_f32_e32 v177, v65, v65
	v_fmac_f32_e32 v177, v64, v64
	v_mul_f32_e32 v233, v59, v59
	v_fmac_f32_e32 v233, v58, v58
	v_mul_f32_e32 v162, v61, v61
	v_fmac_f32_e32 v162, v60, v60
	v_mul_f32_e32 v163, v63, v63
	v_add_f32_e32 v233, v233, v162
	v_fmac_f32_e32 v163, v62, v62
	v_add_f32_e32 v172, v163, v233
	v_add_f32_e32 v172, v177, v172
	v_add_f32_e32 v90, v172, v90
	s_waitcnt vmcnt(7)
	v_pk_mul_f32 v[60:61], v[60:61], v[204:205]
	v_pk_mul_f32 v[58:59], v[58:59], v[202:203]
	v_pk_mul_f32 v[64:65], v[64:65], v[208:209]
	v_pk_mul_f32 v[62:63], v[62:63], v[206:207]
	v_cvt_pk_bf16_f32 v164, v58, v59
	v_cvt_pk_bf16_f32 v165, v60, v61
	v_cvt_pk_bf16_f32 v166, v62, v63
	v_cvt_pk_bf16_f32 v167, v64, v65
	s_nop 0
	s_nop 0
	v_mfma_f32_16x16x32_bf16 v[66:69], v[164:167], v[182:185], v[66:69]
	v_mfma_f32_16x16x32_bf16 v[78:81], v[164:167], v[186:189], v[78:81]
	v_mfma_f32_16x16x32_bf16 v[74:77], v[164:167], v[190:193], v[74:77]
	v_mfma_f32_16x16x32_bf16 v[70:73], v[164:167], v[194:197], v[70:73]
	v_mfma_f32_16x16x32_bf16 v[82:85], v[164:167], v[198:201], v[82:85]
	v_mul_f32_e32 v177, v55, v55
	v_mul_f32_e32 v233, v57, v57
	v_fmac_f32_e32 v177, v54, v54
	v_fmac_f32_e32 v233, v56, v56
	v_add_f32_e32 v177, v177, v233
	v_mul_f32_e32 v233, v51, v51
	v_fmac_f32_e32 v233, v50, v50
	v_add_f32_e32 v177, v233, v177
	v_mul_f32_e32 v233, v53, v53
	v_fmac_f32_e32 v233, v52, v52
	s_waitcnt vmcnt(0)
	v_pk_mul_f32 v[56:57], v[56:57], v[248:249]
	v_pk_mul_f32 v[54:55], v[54:55], v[246:247]
	v_pk_mul_f32 v[52:53], v[52:53], v[252:253]
	v_pk_mul_f32 v[50:51], v[50:51], v[250:251]
	v_cvt_pk_bf16_f32 v164, v54, v55
	v_cvt_pk_bf16_f32 v165, v56, v57
	v_cvt_pk_bf16_f32 v166, v50, v51
	v_cvt_pk_bf16_f32 v167, v52, v53
	v_add_f32_e32 v177, v233, v177
	v_add_f32_e32 v90, v177, v90
	v_mfma_f32_16x16x32_bf16 v[66:69], v[164:167], v[210:213], v[66:69]
	v_mfma_f32_16x16x32_bf16 v[78:81], v[164:167], v[214:217], v[78:81]
	v_mfma_f32_16x16x32_bf16 v[74:77], v[164:167], v[234:237], v[74:77]
	v_mfma_f32_16x16x32_bf16 v[70:73], v[164:167], v[238:241], v[70:73]
	v_mfma_f32_16x16x32_bf16 v[82:85], v[164:167], v[242:245], v[82:85]
	s_add_i32 s32, s1, s0
	s_cmpk_gt_i32 s32, 0x203
	s_cbranch_scc1 .Lrouter_no_next
	v_lshl_or_b32 v190, s32, 4, v97
	v_ashrrev_i32_e32 v191, 31, v190
	v_lshlrev_b64 v[190:191], 13, v[190:191]
	v_lshl_add_u64 v[190:191], v[92:93], 0, v[190:191]
	global_load_dwordx4 v[110:113], v[190:191], off offset:16
	global_load_dwordx4 v[114:117], v[190:191], off
	global_load_dwordx4 v[118:121], v[190:191], off offset:144
	global_load_dwordx4 v[122:125], v[190:191], off offset:128
	global_load_dwordx4 v[126:129], v[190:191], off offset:272
	global_load_dwordx4 v[130:133], v[190:191], off offset:256
	global_load_dwordx4 v[134:137], v[190:191], off offset:400
	global_load_dwordx4 v[138:141], v[190:191], off offset:384
	global_load_dwordx4 v[142:145], v[190:191], off offset:528
	global_load_dwordx4 v[146:149], v[190:191], off offset:512
	global_load_dwordx4 v[150:153], v[190:191], off offset:656
	global_load_dwordx4 v[154:157], v[190:191], off offset:640
	global_load_dwordx4 v[186:189], v[190:191], off offset:784
	global_load_dwordx4 v[182:185], v[190:191], off offset:768
	global_load_dwordx4 v[158:161], v[190:191], off offset:912
	global_load_dwordx4 v[178:181], v[190:191], off offset:896
.Lrouter_no_next:
	ds_bpermute_b32 v164, v87, v90
	s_waitcnt lgkmcnt(0)
	v_add_f32_e32 v90, v90, v164
	ds_bpermute_b32 v177, v174, v90
	s_and_saveexec_b64 s[2:3], s[38:39]
	s_cbranch_execz .LBB0_1647
	s_waitcnt lgkmcnt(0)
	v_add_f32_e32 v90, v90, v177
	ds_write_b32 v175, v90 offset:40960

; DI unsigned pk2(float a, float b) { f32x2 v = {a, b}; bf16x2_t r = __builtin_convertvector(v, bf16x2_t); return __builtin_bit_cast(unsigned, r); }
; #define RT_LOADH(tile_) do { const float* hp_ = H + (size_t)((tile_) * 16 + n) * D + wave * 256 + 8 * q; _Pragma("unroll") for (int ks = 0; ks < 8; ++ks) { hv[ks][0] = *(const f32x4*)(hp_ + ks * 32); hv[ks][1] = *(const f32x4*)(hp_ + ks * 32 + 4); } } while (0)
; DI void phase_router(const Args& a, int l, LAS unsigned char* lds, int wave, int lane, int bid, int G, bool dummy = false) {
;     ...
;         { const float rstd = rs[n]; bf16* up = U + (size_t)(row0 + n) * D + wave * 256 + 8 * q;
; #pragma unroll
;           for (int ks = 0; ks < 8; ++ks) { const f32x4 y0 = hv[ks][0] * rstd, y1 = hv[ks][1] * rstd;
;               *(u32x4*)(up + ks * 32) = (u32x4){pk2(y0[0], y0[1]), pk2(y0[2], y0[3]), pk2(y1[0], y1[1]), pk2(y1[2], y1[3])}; } }
;         if (tile + G < T / 16) RT_LOADH(tile + G);
.LBB0_1652:
	s_or_b64 exec, exec, s[28:29]
	ds_read_b32 v70, v176 offset:46080
	s_lshl_b32 s7, s1, 4
	v_or_b32_e32 v66, s7, v97
	v_ashrrev_i32_e32 v67, 31, v66
	v_lshlrev_b64 v[66:67], 12, v[66:67]
	v_lshl_add_u64 v[72:73], v[88:89], 0, v[66:67]
	s_waitcnt lgkmcnt(0)
	v_pk_mul_f32 v[68:69], v[8:9], v[70:71] op_sel_hi:[1,0]
	v_pk_mul_f32 v[66:67], v[6:7], v[70:71] op_sel_hi:[1,0]
	v_pk_mul_f32 v[74:75], v[4:5], v[70:71] op_sel_hi:[1,0]
	v_pk_mul_f32 v[76:77], v[2:3], v[70:71] op_sel_hi:[1,0]
	v_cvt_pk_bf16_f32 v66, v66, v67
	v_cvt_pk_bf16_f32 v67, v68, v69
	v_cvt_pk_bf16_f32 v68, v76, v77
	v_cvt_pk_bf16_f32 v69, v74, v75
	global_store_dwordx4 v[72:73], v[66:69], off
	v_pk_mul_f32 v[74:75], v[12:13], v[70:71] op_sel_hi:[1,0]
	v_pk_mul_f32 v[76:77], v[10:11], v[70:71] op_sel_hi:[1,0]
	v_pk_mul_f32 v[68:69], v[16:17], v[70:71] op_sel_hi:[1,0]
	v_pk_mul_f32 v[66:67], v[14:15], v[70:71] op_sel_hi:[1,0]
	s_add_i32 s1, s1, s0
	v_cvt_pk_bf16_f32 v66, v66, v67
	v_cvt_pk_bf16_f32 v67, v68, v69
	v_cvt_pk_bf16_f32 v68, v76, v77
	v_cvt_pk_bf16_f32 v69, v74, v75
	global_store_dwordx4 v[72:73], v[66:69], off offset:64
	v_pk_mul_f32 v[74:75], v[20:21], v[70:71] op_sel_hi:[1,0]
	v_pk_mul_f32 v[76:77], v[18:19], v[70:71] op_sel_hi:[1,0]
	v_pk_mul_f32 v[68:69], v[24:25], v[70:71] op_sel_hi:[1,0]
	v_pk_mul_f32 v[66:67], v[22:23], v[70:71] op_sel_hi:[1,0]
	s_cmpk_gt_i32 s1, 0x203
	v_cvt_pk_bf16_f32 v66, v66, v67
	v_cvt_pk_bf16_f32 v67, v68, v69
	v_cvt_pk_bf16_f32 v68, v76, v77
	v_cvt_pk_bf16_f32 v69, v74, v75
	global_store_dwordx4 v[72:73], v[66:69], off offset:128
	v_pk_mul_f32 v[74:75], v[28:29], v[70:71] op_sel_hi:[1,0]
	v_pk_mul_f32 v[76:77], v[26:27], v[70:71] op_sel_hi:[1,0]
	v_pk_mul_f32 v[68:69], v[32:33], v[70:71] op_sel_hi:[1,0]
	v_pk_mul_f32 v[66:67], v[30:31], v[70:71] op_sel_hi:[1,0]
	s_cselect_b64 s[28:29], -1, 0
	v_cvt_pk_bf16_f32 v66, v66, v67
	v_cvt_pk_bf16_f32 v67, v68, v69
	v_cvt_pk_bf16_f32 v68, v76, v77
	v_cvt_pk_bf16_f32 v69, v74, v75
	global_store_dwordx4 v[72:73], v[66:69], off offset:192
	v_pk_mul_f32 v[74:75], v[36:37], v[70:71] op_sel_hi:[1,0]
	v_pk_mul_f32 v[76:77], v[34:35], v[70:71] op_sel_hi:[1,0]
	v_pk_mul_f32 v[68:69], v[40:41], v[70:71] op_sel_hi:[1,0]
	v_pk_mul_f32 v[66:67], v[38:39], v[70:71] op_sel_hi:[1,0]
	s_cmpk_lt_i32 s1, 0x204
	v_cvt_pk_bf16_f32 v66, v66, v67
	v_cvt_pk_bf16_f32 v67, v68, v69
	v_cvt_pk_bf16_f32 v68, v76, v77
	v_cvt_pk_bf16_f32 v69, v74, v75
	global_store_dwordx4 v[72:73], v[66:69], off offset:256
	v_pk_mul_f32 v[74:75], v[44:45], v[70:71] op_sel_hi:[1,0]
	v_pk_mul_f32 v[76:77], v[42:43], v[70:71] op_sel_hi:[1,0]
	v_pk_mul_f32 v[68:69], v[48:49], v[70:71] op_sel_hi:[1,0]
	v_pk_mul_f32 v[66:67], v[46:47], v[70:71] op_sel_hi:[1,0]
	s_nop 0
	v_cvt_pk_bf16_f32 v66, v66, v67
	v_cvt_pk_bf16_f32 v67, v68, v69
	v_cvt_pk_bf16_f32 v68, v76, v77
	v_cvt_pk_bf16_f32 v69, v74, v75
	global_store_dwordx4 v[72:73], v[66:69], off offset:320
	v_pk_mul_f32 v[74:75], v[64:65], v[70:71] op_sel_hi:[1,0]
	v_pk_mul_f32 v[76:77], v[62:63], v[70:71] op_sel_hi:[1,0]
	v_pk_mul_f32 v[68:69], v[60:61], v[70:71] op_sel_hi:[1,0]
	v_pk_mul_f32 v[66:67], v[58:59], v[70:71] op_sel_hi:[1,0]
	s_nop 0
	v_cvt_pk_bf16_f32 v66, v66, v67
	v_cvt_pk_bf16_f32 v67, v68, v69
	v_cvt_pk_bf16_f32 v68, v76, v77
	v_cvt_pk_bf16_f32 v69, v74, v75
	global_store_dwordx4 v[72:73], v[66:69], off offset:384
	v_pk_mul_f32 v[74:75], v[52:53], v[70:71] op_sel_hi:[1,0]
	s_nop 0
	v_pk_mul_f32 v[68:69], v[56:57], v[70:71] op_sel_hi:[1,0]
	v_pk_mul_f32 v[66:67], v[54:55], v[70:71] op_sel_hi:[1,0]
	v_pk_mul_f32 v[70:71], v[50:51], v[70:71] op_sel_hi:[1,0]
	v_cvt_pk_bf16_f32 v66, v66, v67
	v_cvt_pk_bf16_f32 v67, v68, v69
	v_cvt_pk_bf16_f32 v68, v70, v71
	v_cvt_pk_bf16_f32 v69, v74, v75
	global_store_dwordx4 v[72:73], v[66:69], off offset:448
; #define LAS __attribute__((address_space(3)))
; #define RT_LOADH(tile_) do { const float* hp_ = H + (size_t)((tile_) * 16 + n) * D + wave * 256 + 8 * q; _Pragma("unroll") for (int ks = 0; ks < 8; ++ks) { hv[ks][0] = *(const f32x4*)(hp_ + ks * 32); hv[ks][1] = *(const f32x4*)(hp_ + ks * 32 + 4); } } while (0)
; DI void phase_router(const Args& a, int l, LAS unsigned char* lds, int wave, int lane, int bid, int G, bool dummy = false) {
;     ...
;         if (tile + G < T / 16) RT_LOADH(tile + G);
;         asm volatile("s_waitcnt lgkmcnt(0)" ::: "memory"); __builtin_amdgcn_s_barrier(); asm volatile("" ::: "memory");
;         if (tid < 16) { const int m = row0 + tid; const LAS float* p = lg + tid * 72;
;             int gi = 0; float gm = p[0];
; #pragma unroll
;             for (int j = 1; j < 8; ++j) if (p[j] > gm) { gm = p[j]; gi = j; }
;             float se = 0.f;
; #pragma unroll
;             for (int j = 0; j < 8; ++j) se += __expf(p[j] - gm);
;             const float pgrp = 1.f / se;
;             const LAS float* f = p + 8 + gi * 8;
;             int i0 = 0; float f0 = f[0];
; #pragma unroll
;             for (int j = 1; j < 8; ++j) if (f[j] > f0) { f0 = f[j]; i0 = j; }
;             int i1 = -1; float f1 = -3.0e38f;
; #pragma unroll
;             for (int j = 0; j < 8; ++j) if (j != i0 && f[j] > f1) { f1 = f[j]; i1 = j; }
.LBB0_1654:
	s_waitcnt lgkmcnt(0)
	s_barrier
	s_and_saveexec_b64 s[30:31], s[40:41]
	s_cbranch_execz .LBB0_1644
	ds_read_b128 v[70:73], v98 offset:41472
	ds_read_b128 v[66:69], v98 offset:41488
	s_mov_b32 s2, 0xff61b1e6
	s_waitcnt lgkmcnt(1)
	v_cmp_gt_f32_e32 vcc, v71, v70
	s_nop 1
	v_cndmask_b32_e32 v74, v70, v71, vcc
	v_cmp_gt_f32_e64 s[44:45], v72, v74
	s_nop 1
	v_cndmask_b32_e64 v74, v74, v72, s[44:45]
	v_cmp_gt_f32_e64 s[46:47], v73, v74
	s_nop 1
	v_cndmask_b32_e64 v74, v74, v73, s[46:47]
	s_waitcnt lgkmcnt(0)
	v_cmp_gt_f32_e64 s[48:49], v66, v74
	s_nop 1
	v_cndmask_b32_e64 v74, v74, v66, s[48:49]
	v_cmp_gt_f32_e64 s[50:51], v67, v74
	s_nop 1
	v_cndmask_b32_e64 v74, v74, v67, s[50:51]
	v_cmp_gt_f32_e64 s[52:53], v68, v74
	s_nop 1
	v_cndmask_b32_e64 v79, v74, v68, s[52:53]
	v_cndmask_b32_e64 v74, 0, 8, vcc
	v_cndmask_b32_e64 v74, v74, 16, s[44:45]
	v_cndmask_b32_e64 v74, v74, 24, s[46:47]
	v_cndmask_b32_e64 v74, v74, 32, s[48:49]
	v_cndmask_b32_e64 v74, v74, 40, s[50:51]
	v_cndmask_b32_e64 v74, v74, 48, s[52:53]
	v_cmp_gt_f32_e32 vcc, v69, v79
	s_nop 1
	v_cndmask_b32_e64 v76, v74, 56, vcc
	v_lshl_add_u32 v74, v76, 2, v98
	v_add_u32_e32 v75, 0xa220, v74
	ds_read2_b32 v[82:83], v75 offset1:1
	v_add_u32_e32 v75, 0xa228, v74
	v_add_u32_e32 v77, 0xa230, v74
	v_add_u32_e32 v74, 0xa238, v74
	ds_read2_b32 v[84:85], v75 offset1:1
	ds_read2_b32 v[164:165], v77 offset1:1
	ds_read2_b32 v[74:75], v74 offset1:1
	s_waitcnt lgkmcnt(3)
	v_cmp_gt_f32_e64 s[44:45], v83, v82
	v_cmp_nlt_f32_e64 s[52:53], s2, v82
	s_nop 0
	v_cndmask_b32_e64 v78, v82, v83, s[44:45]
	v_cndmask_b32_e64 v77, 0, 1, s[44:45]
	s_waitcnt lgkmcnt(2)
	v_cmp_gt_f32_e64 s[44:45], v84, v78
	s_nop 1
	v_cndmask_b32_e64 v78, v78, v84, s[44:45]
	v_cndmask_b32_e64 v77, v77, 2, s[44:45]
	v_cmp_gt_f32_e64 s[44:45], v85, v78
	s_nop 1
	v_cndmask_b32_e64 v78, v78, v85, s[44:45]
	v_cndmask_b32_e64 v77, v77, 3, s[44:45]
	s_waitcnt lgkmcnt(1)
	v_cmp_gt_f32_e64 s[44:45], v164, v78
	s_nop 1
	v_cndmask_b32_e64 v78, v78, v164, s[44:45]
	v_cndmask_b32_e64 v77, v77, 4, s[44:45]
	v_cmp_gt_f32_e64 s[44:45], v165, v78
	s_nop 1
	v_cndmask_b32_e64 v78, v78, v165, s[44:45]
	v_cndmask_b32_e64 v77, v77, 5, s[44:45]
	s_waitcnt lgkmcnt(0)
	v_cmp_ngt_f32_e64 s[44:45], v74, v78
	s_nop 1
	v_cndmask_b32_e64 v80, v74, v78, s[44:45]
	v_cndmask_b32_e64 v77, 6, v77, s[44:45]
	v_cmp_gt_f32_e64 s[48:49], v75, v80
	s_or_b64 s[2:3], s[44:45], s[48:49]
	v_cmp_ngt_f32_e64 s[46:47], v75, v80
	v_cndmask_b32_e64 v77, v77, 7, s[48:49]
	v_cmp_eq_u32_e64 s[50:51], 0, v77
	s_or_b64 s[50:51], s[50:51], s[52:53]
	s_nop 0
	v_cndmask_b32_e64 v81, v82, v232, s[50:51]
	v_cndmask_b32_e64 v78, 0, -1, s[50:51]
	v_cmp_ne_u32_e64 s[50:51], 1, v77
	v_cmp_gt_f32_e64 s[52:53], v83, v81
	s_and_b64 s[50:51], s[50:51], s[52:53]
	v_cndmask_b32_e64 v81, v81, v83, s[50:51]
	v_cndmask_b32_e64 v78, v78, 1, s[50:51]
	v_cmp_ne_u32_e64 s[50:51], 2, v77
	v_cmp_gt_f32_e64 s[52:53], v84, v81
	s_and_b64 s[50:51], s[50:51], s[52:53]
	v_cndmask_b32_e64 v81, v81, v84, s[50:51]
	v_cndmask_b32_e64 v78, v78, 2, s[50:51]
	v_cmp_ne_u32_e64 s[50:51], 3, v77
	v_cmp_gt_f32_e64 s[52:53], v85, v81
	s_and_b64 s[50:51], s[50:51], s[52:53]
	v_cndmask_b32_e64 v81, v81, v85, s[50:51]
	v_cndmask_b32_e64 v78, v78, 3, s[50:51]
	v_cmp_ne_u32_e64 s[50:51], 4, v77
	v_cmp_gt_f32_e64 s[52:53], v164, v81
	s_and_b64 s[50:51], s[50:51], s[52:53]
	v_cndmask_b32_e64 v81, v81, v164, s[50:51]
	v_cndmask_b32_e64 v78, v78, 4, s[50:51]
	v_cmp_ne_u32_e64 s[50:51], 5, v77
	v_cmp_gt_f32_e64 s[52:53], v165, v81
	s_and_b64 s[50:51], s[50:51], s[52:53]
	v_cndmask_b32_e64 v81, v81, v165, s[50:51]
	v_cmp_gt_f32_e64 s[44:45], v74, v81
	v_cndmask_b32_e64 v78, v78, 5, s[50:51]
	s_and_b64 s[44:45], s[2:3], s[44:45]
	v_cndmask_b32_e64 v78, v78, 6, s[44:45]
	v_cndmask_b32_e64 v74, v81, v74, s[44:45]
	s_and_saveexec_b64 s[2:3], s[46:47]
	s_cbranch_execz .LBB0_1643
	v_cmp_gt_f32_e64 s[44:45], v75, v74
	s_and_saveexec_b64 s[34:35], s[44:45]
	s_cbranch_execz .LBB0_1642
	v_mov_b32_e32 v78, 7
	v_mov_b32_e32 v74, v75
	s_branch .LBB0_1642
